# RWKV scan wave loop rewritten by hand: the two row-group chains interleaved stage by stage, next record's flag read and operand reads issued early; same instructions and operands
# baseline (speedup 1.0000x reference)
.LBB0_1011:
	v_lshl_add_u64 v[0:1], s[22:23], 0, v[178:179]
	v_readlane_b32 s8, v251, 4
	v_lshlrev_b64 v[0:1], 11, v[0:1]
	v_readlane_b32 s9, v251, 5
	s_lshl_b32 s92, s1, 7
	s_lshl_b32 s20, s33, 6
	v_lshl_add_u64 v[0:1], s[8:9], 0, v[0:1]
	v_lshl_add_u64 v[0:1], v[0:1], 0, s[92:93]
	s_mov_b32 s21, s93
	v_add_u32_e32 v8, v202, v203
	v_lshl_add_u64 v[0:1], v[0:1], 0, s[20:21]
	v_lshlrev_b32_e32 v128, 1, v176
	v_add_u32_e32 v4, 0x800, v8
	v_add_u32_e32 v9, s20, v205
	v_lshl_add_u64 v[184:185], v[0:1], 0, v[128:129]
	ds_read2_b64 v[0:3], v4 offset1:4
	ds_read2_b64 v[4:7], v4 offset0:8 offset1:12
	ds_read_b64_tr_b16 v[10:11], v9 offset:10496
	ds_read_b64_tr_b16 v[14:15], v9 offset:10528
	ds_read2_b64 v[16:19], v8 offset1:4
	ds_read2_b64 v[20:23], v8 offset0:8 offset1:12
	ds_read_b128 v[24:27], v220 offset:8192
	ds_read_b128 v[28:31], v220 offset:9216
	v_add_u32_e32 v8, 0, v195
	ds_read_b128 v[56:59], v8 offset:10240
	ds_read_b128 v[40:43], v8 offset:10304
	ds_read_b64_tr_b16 v[44:45], v205 offset:4096
	ds_read_b64_tr_b16 v[48:49], v205 offset:4128
	ds_read_b64_tr_b16 v[52:53], v205 offset:4160
	ds_read_b64_tr_b16 v[60:61], v205 offset:4192
	ds_read_b64_tr_b16 v[46:47], v205 offset:6144
	ds_read_b64_tr_b16 v[50:51], v205 offset:6176
	ds_read_b64_tr_b16 v[54:55], v205 offset:6208
	ds_read_b64_tr_b16 v[62:63], v205 offset:6240
	ds_read_b128 v[36:39], v8 offset:10368
	ds_read_b128 v[32:35], v8 offset:10432
	v_mov_b32_e32 v100, 0
	s_mov_b32 s8, 0
	v_mov_b32_e32 v101, v100
	v_mov_b32_e32 v102, v100
	v_mov_b32_e32 v103, v100
	v_mov_b32_e32 v96, v100
	v_mov_b32_e32 v97, v100
	v_mov_b32_e32 v98, v100
	v_mov_b32_e32 v99, v100
	v_mov_b32_e32 v108, v100
	v_mov_b32_e32 v109, v100
	v_mov_b32_e32 v110, v100
	v_mov_b32_e32 v111, v100
	v_mov_b32_e32 v112, v100
	v_mov_b32_e32 v113, v100
	v_mov_b32_e32 v114, v100
	v_mov_b32_e32 v115, v100
	v_mov_b32_e32 v84, v100
	v_mov_b32_e32 v85, v100
	v_mov_b32_e32 v86, v100
	v_mov_b32_e32 v87, v100
	v_mov_b32_e32 v72, v100
	v_mov_b32_e32 v73, v100
	v_mov_b32_e32 v74, v100
	v_mov_b32_e32 v75, v100
	v_mov_b32_e32 v88, v100
	v_mov_b32_e32 v89, v100
	v_mov_b32_e32 v90, v100
	v_mov_b32_e32 v91, v100
	v_mov_b32_e32 v80, v100
	v_mov_b32_e32 v81, v100
	v_mov_b32_e32 v82, v100
	v_mov_b32_e32 v83, v100
	v_readlane_b32 s1, v254, 3
	s_mov_b32 s8, 0
	s_mov_b32 s21, 1
	s_nop 1
	v_mov_b32_e32 v128, s1
.Lrs_a:
	s_waitcnt lgkmcnt(0)
	s_add_i32 s9, s8, 1
	v_mov_b32_e32 v170, s9
	s_and_saveexec_b64 s[22:23], s[36:37]
	ds_write_b32 v128, v170 offset:48
	s_mov_b64 exec, s[22:23]
	s_lshl_b32 s1, s21, 2
	s_add_i32 s1, s1, 0x1fa00
	v_mov_b32_e32 v180, s1
	ds_read_b32 v180, v180
	s_add_i32 s1, s8, 2
	s_mul_i32 s26, s21, 0x3200
	v_cvt_pk_bf16_f32 v222, v100, v101
	v_cvt_pk_bf16_f32 v223, v102, v103
	v_cvt_pk_bf16_f32 v224, v96, v97
	v_cvt_pk_bf16_f32 v225, v98, v99
	v_cvt_pk_bf16_f32 v226, v108, v109
	v_cvt_pk_bf16_f32 v227, v110, v111
	v_cvt_pk_bf16_f32 v228, v112, v113
	v_cvt_pk_bf16_f32 v229, v114, v115
	v_cvt_pk_bf16_f32 v238, v84, v85
	v_cvt_pk_bf16_f32 v239, v86, v87
	v_cvt_pk_bf16_f32 v240, v72, v73
	v_cvt_pk_bf16_f32 v241, v74, v75
	v_cvt_pk_bf16_f32 v242, v88, v89
	v_cvt_pk_bf16_f32 v243, v90, v91
	v_cvt_pk_bf16_f32 v244, v80, v81
	v_cvt_pk_bf16_f32 v245, v82, v83
	v_mfma_f32_16x16x32_bf16 v[230:233], v[16:19], v[222:225], 0
	v_mfma_f32_16x16x32_bf16 v[234:237], v[0:3], v[222:225], 0
	v_mfma_f32_16x16x32_bf16 v[246:249], v[16:19], v[238:241], 0
	v_mfma_f32_16x16x32_bf16 v[162:165], v[0:3], v[238:241], 0
	v_mfma_f32_16x16x32_bf16 v[230:233], v[20:23], v[226:229], v[230:233]
	v_mfma_f32_16x16x32_bf16 v[246:249], v[20:23], v[242:245], v[246:249]
	v_mfma_f32_16x16x32_bf16 v[234:237], v[4:7], v[226:229], v[234:237]
	v_mfma_f32_16x16x32_bf16 v[162:165], v[4:7], v[242:245], v[162:165]
	s_lshl_b32 s92, s8, 15
	v_lshl_add_u64 v[166:167], v[184:185], 0, s[92:93]
	s_add_i32 s92, s92, 0x1000
	v_lshl_add_u64 v[168:169], v[184:185], 0, s[92:93]
	s_nop 3
	v_cvt_pk_bf16_f32 v8, v230, v231
	v_cvt_pk_bf16_f32 v9, v232, v233
	v_cvt_pk_bf16_f32 v12, v246, v247
	v_cvt_pk_bf16_f32 v13, v248, v249
	s_nop 0
	v_mfma_f32_16x16x32_bf16 v[230:233], v[24:27], v[8:11], 0
	v_mfma_f32_16x16x32_bf16 v[246:249], v[24:27], v[12:15], 0
	s_cmp_gt_u32 s8, 0x1000
	s_cbranch_scc1 .Lrs_a_nold
	s_waitcnt lgkmcnt(0)
	v_cmp_eq_u32_e32 vcc, s1, v180
	s_cbranch_vccnz .Lrs_a_rdy
	s_mov_b32 s27, 0x400000
.Lrs_a_spin:
	s_sleep 1
	s_lshl_b32 s9, s21, 2
	s_add_i32 s9, s9, 0x1fa00
	v_mov_b32_e32 v180, s9
	ds_read_b32 v180, v180
	s_add_i32 s27, s27, -1
	s_cmp_eq_u32 s27, 0
	s_cbranch_scc1 .Lrs_a_rdy
	s_waitcnt lgkmcnt(0)
	v_cmp_eq_u32_e32 vcc, s1, v180
	s_cbranch_vccz .Lrs_a_spin
.Lrs_a_rdy:
	v_add3_u32 v181, s26, v194, v203
	ds_read2_b64 v[116:119], v181 offset1:4
	ds_read2_b64 v[120:123], v181 offset0:8 offset1:12
	v_add_u32_e32 v181, 0x800, v181
	ds_read2_b64 v[104:107], v181 offset1:4
	ds_read2_b64 v[92:95], v181 offset0:8 offset1:12
	v_add3_u32 v182, s26, v204, v191
	v_add_u32_e32 v183, s20, v182
	ds_read_b64_tr_b16 v[66:67], v183 offset:10496
	ds_read_b64_tr_b16 v[70:71], v183 offset:10528
.Lrs_a_c1:
	v_cvt_pk_bf16_f32 v8, v230, v231
	v_cvt_pk_bf16_f32 v9, v232, v233
	v_cvt_pk_bf16_f32 v12, v246, v247
	v_cvt_pk_bf16_f32 v13, v248, v249
	s_nop 0
	v_mfma_f32_16x16x32_bf16 v[234:237], v[28:31], v[8:11], v[234:237]
	v_mfma_f32_16x16x32_bf16 v[100:103], v[44:47], v[8:11], v[100:103]
	v_mfma_f32_16x16x32_bf16 v[96:99], v[48:51], v[8:11], v[96:99]
	v_mfma_f32_16x16x32_bf16 v[108:111], v[52:55], v[8:11], v[108:111]
	v_mfma_f32_16x16x32_bf16 v[112:115], v[60:63], v[8:11], v[112:115]
	v_mfma_f32_16x16x32_bf16 v[162:165], v[28:31], v[12:15], v[162:165]
	v_mfma_f32_16x16x32_bf16 v[84:87], v[44:47], v[12:15], v[84:87]
	v_mfma_f32_16x16x32_bf16 v[72:75], v[48:51], v[12:15], v[72:75]
	v_mfma_f32_16x16x32_bf16 v[88:91], v[52:55], v[12:15], v[88:91]
	v_mfma_f32_16x16x32_bf16 v[80:83], v[60:63], v[12:15], v[80:83]
	v_cvt_pk_bf16_f32 v170, v234, v235
	v_cvt_pk_bf16_f32 v171, v236, v237
	v_pk_mul_f32 v[100:101], v[100:101], v[56:57]
	v_pk_mul_f32 v[102:103], v[102:103], v[58:59]
	v_pk_mul_f32 v[96:97], v[96:97], v[40:41]
	v_pk_mul_f32 v[98:99], v[98:99], v[42:43]
	v_pk_mul_f32 v[108:109], v[108:109], v[36:37]
	v_pk_mul_f32 v[110:111], v[110:111], v[38:39]
	v_pk_mul_f32 v[112:113], v[112:113], v[32:33]
	v_pk_mul_f32 v[114:115], v[114:115], v[34:35]
	global_store_short v[166:167], v170, off
	global_store_short_d16_hi v[166:167], v170, off offset:2048
	global_store_short v[168:169], v171, off
	global_store_short_d16_hi v[168:169], v171, off offset:2048
	v_cvt_pk_bf16_f32 v172, v162, v163
	v_cvt_pk_bf16_f32 v173, v164, v165
	v_pk_mul_f32 v[84:85], v[84:85], v[56:57]
	v_pk_mul_f32 v[86:87], v[86:87], v[58:59]
	v_pk_mul_f32 v[72:73], v[72:73], v[40:41]
	v_pk_mul_f32 v[74:75], v[74:75], v[42:43]
	v_pk_mul_f32 v[88:89], v[88:89], v[36:37]
	v_pk_mul_f32 v[90:91], v[90:91], v[38:39]
	v_pk_mul_f32 v[80:81], v[80:81], v[32:33]
	v_pk_mul_f32 v[82:83], v[82:83], v[34:35]
	global_store_short v[166:167], v172, off offset:32
	global_store_short_d16_hi v[166:167], v172, off offset:2080
	global_store_short v[168:169], v173, off offset:32
	global_store_short_d16_hi v[168:169], v173, off offset:2080
	s_cmp_gt_u32 s8, 0x1000
	s_cbranch_scc1 .Lrs_a_end
	ds_read_b64_tr_b16 v[130:131], v182 offset:4096
	ds_read_b64_tr_b16 v[134:135], v182 offset:4128
	ds_read_b64_tr_b16 v[138:139], v182 offset:4160
	ds_read_b64_tr_b16 v[142:143], v182 offset:4192
	ds_read_b64_tr_b16 v[132:133], v182 offset:6144
	ds_read_b64_tr_b16 v[136:137], v182 offset:6176
	ds_read_b64_tr_b16 v[140:141], v182 offset:6208
	ds_read_b64_tr_b16 v[144:145], v182 offset:6240
	v_add_u32_e32 v181, s26, v195
	ds_read_b128 v[146:149], v181 offset:10240
	ds_read_b128 v[150:153], v181 offset:10304
	ds_read_b128 v[154:157], v181 offset:10368
	ds_read_b128 v[158:161], v181 offset:10432
	v_add_u32_e32 v181, v181, v196
	ds_read_b128 v[76:79], v181 offset:8192
	ds_read_b128 v[124:127], v181 offset:9216
	s_add_i32 s21, s21, 1
	s_cmp_eq_u32 s21, 10
	s_cselect_b32 s21, 0, s21

.Lrs_b:
	s_waitcnt lgkmcnt(0)
	s_add_i32 s9, s8, 1
	v_mov_b32_e32 v170, s9
	s_and_saveexec_b64 s[22:23], s[36:37]
	ds_write_b32 v128, v170 offset:48
	s_mov_b64 exec, s[22:23]
	s_lshl_b32 s1, s21, 2
	s_add_i32 s1, s1, 0x1fa00
	v_mov_b32_e32 v180, s1
	ds_read_b32 v180, v180
	s_add_i32 s1, s8, 2
	s_mul_i32 s26, s21, 0x3200
	v_cvt_pk_bf16_f32 v222, v100, v101
	v_cvt_pk_bf16_f32 v223, v102, v103
	v_cvt_pk_bf16_f32 v224, v96, v97
	v_cvt_pk_bf16_f32 v225, v98, v99
	v_cvt_pk_bf16_f32 v226, v108, v109
	v_cvt_pk_bf16_f32 v227, v110, v111
	v_cvt_pk_bf16_f32 v228, v112, v113
	v_cvt_pk_bf16_f32 v229, v114, v115
	v_cvt_pk_bf16_f32 v238, v84, v85
	v_cvt_pk_bf16_f32 v239, v86, v87
	v_cvt_pk_bf16_f32 v240, v72, v73
	v_cvt_pk_bf16_f32 v241, v74, v75
	v_cvt_pk_bf16_f32 v242, v88, v89
	v_cvt_pk_bf16_f32 v243, v90, v91
	v_cvt_pk_bf16_f32 v244, v80, v81
	v_cvt_pk_bf16_f32 v245, v82, v83
	v_mfma_f32_16x16x32_bf16 v[230:233], v[116:119], v[222:225], 0
	v_mfma_f32_16x16x32_bf16 v[234:237], v[104:107], v[222:225], 0
	v_mfma_f32_16x16x32_bf16 v[246:249], v[116:119], v[238:241], 0
	v_mfma_f32_16x16x32_bf16 v[162:165], v[104:107], v[238:241], 0
	v_mfma_f32_16x16x32_bf16 v[230:233], v[120:123], v[226:229], v[230:233]
	v_mfma_f32_16x16x32_bf16 v[246:249], v[120:123], v[242:245], v[246:249]
	v_mfma_f32_16x16x32_bf16 v[234:237], v[92:95], v[226:229], v[234:237]
	v_mfma_f32_16x16x32_bf16 v[162:165], v[92:95], v[242:245], v[162:165]
	s_lshl_b32 s92, s8, 15
	v_lshl_add_u64 v[166:167], v[184:185], 0, s[92:93]
	s_add_i32 s92, s92, 0x1000
	v_lshl_add_u64 v[168:169], v[184:185], 0, s[92:93]
	s_nop 3
	v_cvt_pk_bf16_f32 v64, v230, v231
	v_cvt_pk_bf16_f32 v65, v232, v233
	v_cvt_pk_bf16_f32 v68, v246, v247
	v_cvt_pk_bf16_f32 v69, v248, v249
	s_nop 0
	v_mfma_f32_16x16x32_bf16 v[230:233], v[76:79], v[64:67], 0
	v_mfma_f32_16x16x32_bf16 v[246:249], v[76:79], v[68:71], 0
	s_cmp_gt_u32 s8, 0xfe
	s_cbranch_scc1 .Lrs_b_nold
	s_waitcnt lgkmcnt(0)
	v_cmp_eq_u32_e32 vcc, s1, v180
	s_cbranch_vccnz .Lrs_b_rdy
	s_mov_b32 s27, 0x400000

.Lrs_b_rdy:
	v_add3_u32 v181, s26, v194, v203
	ds_read2_b64 v[16:19], v181 offset1:4
	ds_read2_b64 v[20:23], v181 offset0:8 offset1:12
	v_add_u32_e32 v181, 0x800, v181
	ds_read2_b64 v[0:3], v181 offset1:4
	ds_read2_b64 v[4:7], v181 offset0:8 offset1:12
	v_add3_u32 v182, s26, v204, v191
	v_add_u32_e32 v183, s20, v182
	ds_read_b64_tr_b16 v[10:11], v183 offset:10496
	ds_read_b64_tr_b16 v[14:15], v183 offset:10528
.Lrs_b_c1:
	v_cvt_pk_bf16_f32 v64, v230, v231
	v_cvt_pk_bf16_f32 v65, v232, v233
	v_cvt_pk_bf16_f32 v68, v246, v247
	v_cvt_pk_bf16_f32 v69, v248, v249
	s_nop 0
	v_mfma_f32_16x16x32_bf16 v[234:237], v[124:127], v[64:67], v[234:237]
	v_mfma_f32_16x16x32_bf16 v[100:103], v[130:133], v[64:67], v[100:103]
	v_mfma_f32_16x16x32_bf16 v[96:99], v[134:137], v[64:67], v[96:99]
	v_mfma_f32_16x16x32_bf16 v[108:111], v[138:141], v[64:67], v[108:111]
	v_mfma_f32_16x16x32_bf16 v[112:115], v[142:145], v[64:67], v[112:115]
	v_mfma_f32_16x16x32_bf16 v[162:165], v[124:127], v[68:71], v[162:165]
	v_mfma_f32_16x16x32_bf16 v[84:87], v[130:133], v[68:71], v[84:87]
	v_mfma_f32_16x16x32_bf16 v[72:75], v[134:137], v[68:71], v[72:75]
	v_mfma_f32_16x16x32_bf16 v[88:91], v[138:141], v[68:71], v[88:91]
	v_mfma_f32_16x16x32_bf16 v[80:83], v[142:145], v[68:71], v[80:83]
	v_cvt_pk_bf16_f32 v170, v234, v235
	v_cvt_pk_bf16_f32 v171, v236, v237
	v_pk_mul_f32 v[100:101], v[100:101], v[146:147]
	v_pk_mul_f32 v[102:103], v[102:103], v[148:149]
	v_pk_mul_f32 v[96:97], v[96:97], v[150:151]
	v_pk_mul_f32 v[98:99], v[98:99], v[152:153]
	v_pk_mul_f32 v[108:109], v[108:109], v[154:155]
	v_pk_mul_f32 v[110:111], v[110:111], v[156:157]
	v_pk_mul_f32 v[112:113], v[112:113], v[158:159]
	v_pk_mul_f32 v[114:115], v[114:115], v[160:161]
	global_store_short v[166:167], v170, off
	global_store_short_d16_hi v[166:167], v170, off offset:2048
	global_store_short v[168:169], v171, off
	global_store_short_d16_hi v[168:169], v171, off offset:2048
	v_cvt_pk_bf16_f32 v172, v162, v163
	v_cvt_pk_bf16_f32 v173, v164, v165
	v_pk_mul_f32 v[84:85], v[84:85], v[146:147]
	v_pk_mul_f32 v[86:87], v[86:87], v[148:149]
	v_pk_mul_f32 v[72:73], v[72:73], v[150:151]
	v_pk_mul_f32 v[74:75], v[74:75], v[152:153]
	v_pk_mul_f32 v[88:89], v[88:89], v[154:155]
	v_pk_mul_f32 v[90:91], v[90:91], v[156:157]
	v_pk_mul_f32 v[80:81], v[80:81], v[158:159]
	v_pk_mul_f32 v[82:83], v[82:83], v[160:161]
	global_store_short v[166:167], v172, off offset:32
	global_store_short_d16_hi v[166:167], v172, off offset:2080
	global_store_short v[168:169], v173, off offset:32
	global_store_short_d16_hi v[168:169], v173, off offset:2080
	s_cmp_gt_u32 s8, 0xfe
	s_cbranch_scc1 .Lrs_b_end
	ds_read_b64_tr_b16 v[44:45], v182 offset:4096
	ds_read_b64_tr_b16 v[48:49], v182 offset:4128
	ds_read_b64_tr_b16 v[52:53], v182 offset:4160
	ds_read_b64_tr_b16 v[60:61], v182 offset:4192
	ds_read_b64_tr_b16 v[46:47], v182 offset:6144
	ds_read_b64_tr_b16 v[50:51], v182 offset:6176
	ds_read_b64_tr_b16 v[54:55], v182 offset:6208
	ds_read_b64_tr_b16 v[62:63], v182 offset:6240
	v_add_u32_e32 v181, s26, v195
	ds_read_b128 v[56:59], v181 offset:10240
	ds_read_b128 v[40:43], v181 offset:10304
	ds_read_b128 v[36:39], v181 offset:10368
	ds_read_b128 v[32:35], v181 offset:10432
	v_add_u32_e32 v181, v181, v196
	ds_read_b128 v[24:27], v181 offset:8192
	ds_read_b128 v[28:31], v181 offset:9216
	s_add_i32 s21, s21, 1
	s_cmp_eq_u32 s21, 10
	s_cselect_b32 s21, 0, s21
.Lrs_b_end:
	s_add_i32 s8, s8, 1
	s_cmp_lt_u32 s8, 0x100
	s_cbranch_scc1 .Lrs_a
	s_branch .LBB0_878
.Lrs_a_nold:
	s_nop 7
	s_branch .Lrs_a_c1
